# v65 + non-temporal hint on attention q-row loads (each read by one unit) and on the PE GEMM's output stores (read once in the PLE phase)
# baseline (speedup 1.0000x reference)
; #define GAS __attribute__((address_space(1)))
; #define LAS __attribute__((address_space(3)))
; #define GAS __attribute__((address_space(1)))
; template <class Tp> __device__ __forceinline__ Tp* wsp(const Frame& F, size_t off) { return (Tp*)(F.ws + off); }
; __device__ __forceinline__ void mla_prologue(LAS unsigned char* lds, int tid, const bf16_t* QM, const bf16_t* KN, const bf16_t* KR, const bf16_t* VM, AU u, bf16x8 (&qr)[6]) {
;     asm volatile("" : "+v"(tid));
;     MLA_ADDR(u)
;     const bf16_t* Qw = QM + (rowb + q0 + wid * 32) * 768 + h * 96;
; #pragma unroll
;     for (int d0 = 0; d0 < 6; ++d0) qr[d0] = *(const GAS bf16x8*)(Qw + (size_t)r32 * 768 + d0 * 16 + hi * 8);
; #pragma unroll
;     for (int j = 0; j < 5; ++j) if (j < NT) mla_issue(lds, wid, ksrc, rsrc, vsrc, j);
; __device__ __forceinline__ void phase_attn(Frame& F) {
;     const bf16_t* QKV = wsp<bf16_t>(F, WS_QKV); bf16_t* OA = wsp<bf16_t>(F, WS_OA); float* OSS = wsp<float>(F, WS_OSS);
;     const bf16_t* QM = wsp<bf16_t>(F, WS_QM); const bf16_t* KN = wsp<bf16_t>(F, WS_KN); const bf16_t* KR = wsp<bf16_t>(F, WS_KR); const bf16_t* VM = wsp<bf16_t>(F, WS_VM);
;     const int vcu = (F.G % 8 == 0) ? (F.bx % 8) * (F.G / 8) + F.bx / 8 : F.bx;
;     { const int nu = vcu < 512 ? 2 * ((512 - vcu + F.G - 1) / F.G) : 0;
;       auto unit = [&](int i) { const int p = vcu + (i >> 1) * F.G, bh = p >> 3, s = p & 7; return att::AU{bh >> 3, bh & 7, (i & 1) ? s : 15 - s}; };
;       if (nu > 0) {
;           bf16x8 qr[6];
;           att::mla_prologue(F.lds, F.tid, QM, KN, KR, VM, unit(0), qr);
.LBB0_765:
	s_add_u32 s6, s74, 0x22800000
	s_addc_u32 s7, s75, 0
	v_writelane_b32 v255, s6, 36
	s_nop 1
	v_writelane_b32 v255, s7, 37
	s_add_u32 s6, s74, 0x26a00000
	s_addc_u32 s7, s75, 0
	v_writelane_b32 v255, s6, 38
	s_cmp_lt_i32 s2, 1
	s_nop 0
	v_writelane_b32 v255, s7, 39
	s_cbranch_scc1 .LBB0_873
	s_add_u32 s33, s74, 0x1b800000
	s_addc_u32 s36, s75, 0
	s_add_u32 s10, s74, 0x1e800000
	s_addc_u32 s11, s75, 0
	v_mov_b32_e32 v6, v188
	s_add_u32 s12, s74, 0x1b600000
	s_addc_u32 s13, s75, 0
	v_readfirstlane_b32 s6, v6
	s_ashr_i32 s18, s6, 6
	s_lshl_b32 s8, s18, 3
	s_lshl_b32 s3, s18, 5
	s_ashr_i32 s9, s8, 31
	s_and_b32 s7, s18, 3
	s_ashr_i32 s14, s3, 31
	v_readlane_b32 s15, v253, 63
	s_add_u32 s3, s15, s3
	v_readlane_b32 s15, v254, 56
	s_addc_u32 s14, s15, s14
	s_mulk_i32 s14, 0x600
	s_mul_hi_u32 s15, s3, 0x600
	s_add_i32 s15, s15, s14
	s_mulk_i32 s3, 0x600
	s_add_u32 s3, s33, s3
	v_and_b32_e32 v0, 31, v6
	s_addc_u32 s15, s36, s15
	v_readlane_b32 s14, v254, 53
	s_add_u32 s14, s3, s14
	v_mul_u32_u24_e32 v0, 0x300, v0
	s_addc_u32 s15, s15, 0
	v_lshlrev_b32_e32 v0, 1, v0
	v_lshl_add_u64 v[2:3], s[14:15], 0, v[0:1]
	v_lshrrev_b32_e32 v0, 1, v6
	v_and_b32_e32 v0, 16, v0
	v_lshl_add_u64 v[2:3], v[2:3], 0, v[0:1]
	global_load_dwordx4 v[96:99], v[2:3], off nt
	global_load_dwordx4 v[100:103], v[2:3], off offset:32 nt
	global_load_dwordx4 v[104:107], v[2:3], off offset:64 nt
	global_load_dwordx4 v[108:111], v[2:3], off offset:96 nt
	global_load_dwordx4 v[112:115], v[2:3], off offset:128 nt
	global_load_dwordx4 v[116:119], v[2:3], off offset:160 nt
	v_readlane_b32 s14, v254, 54
	v_and_b32_e32 v0, 63, v6
	v_readlane_b32 s15, v254, 55
	v_or_b32_e32 v2, s14, v0
	v_readlane_b32 s3, v254, 0
	v_mov_b32_e32 v3, s15
	v_lshlrev_b64 v[4:5], 10, v[2:3]
	v_lshl_add_u64 v[4:5], s[10:11], 0, v[4:5]
	s_lshl_b32 s88, s3, 1
	v_lshl_add_u64 v[4:5], v[4:5], 0, s[88:89]
	v_lshlrev_b64 v[2:3], 6, v[2:3]
	v_lshl_add_u64 v[4:5], s[8:9], 1, v[4:5]
	s_lshl_b32 s8, s7, 4
	s_lshl_b32 s3, s18, 10
	v_lshl_add_u64 v[2:3], s[12:13], 0, v[2:3]
	s_mov_b32 s9, s89
	s_cmp_lt_i32 s18, 4
	v_lshl_add_u64 v[2:3], v[2:3], 0, s[8:9]
	s_cselect_b64 s[16:17], -1, 0
	s_add_i32 s3, s3, 0
	s_mov_b32 s8, m0
	s_mov_b32 m0, s3
	s_nop 0
	global_load_lds_dwordx4 v[4:5], off
	s_mov_b32 m0, s8
	s_cmp_gt_i32 s18, 3
	s_cbranch_scc1 .LBB0_768
	s_add_i32 s8, s3, 0x2000
	s_mov_b32 s9, m0
	s_mov_b32 m0, s8
	s_nop 0
	global_load_lds_dwordx4 v[2:3], off
	s_mov_b32 m0, s9

; #define GAS __attribute__((address_space(1)))
; #define LAS __attribute__((address_space(3)))
; #define GAS __attribute__((address_space(1)))
; __device__ __forceinline__ float xor32(float x) { auto rr = __builtin_amdgcn_permlane32_swap(__float_as_uint(x), __float_as_uint(x), false, false); return __uint_as_float(((unsigned)(threadIdx.x & 32)) ? rr[0] : rr[1]); }
; __device__ __forceinline__ void store_o(bf16_t* orow, const f32x16& o0, const f32x16& o1, int hi, float sc, float* oss) {
;     float sq = 0.f;
; #pragma unroll
;     for (int r = 0; r < 16; ++r) sq += o0[r] * o0[r] + o1[r] * o1[r];
;     sq = (sq + xor32(sq)) * (sc * sc);
;     if (hi == 0) *(GAS float*)oss = sq;
; #pragma unroll
;     for (int half = 0; half < 2; ++half) {
;         const f32x16& o = half ? o1 : o0;
; #pragma unroll
;         for (int k = 0; k < 4; k += 2) {
;             unsigned ax = cvtpk(o[4 * k] * sc, o[4 * k + 1] * sc), ay = cvtpk(o[4 * k + 2] * sc, o[4 * k + 3] * sc);
;             unsigned bx = cvtpk(o[4 * k + 4] * sc, o[4 * k + 5] * sc), by = cvtpk(o[4 * k + 6] * sc, o[4 * k + 7] * sc);
;             { auto r = __builtin_amdgcn_permlane32_swap(ax, bx, false, false); ax = r[0]; bx = r[1]; }
;             { auto r = __builtin_amdgcn_permlane32_swap(ay, by, false, false); ay = r[0]; by = r[1]; }
;             *(GAS u32x4*)(orow + 32 * half + 8 * k + 8 * hi) = (u32x4){ax, ay, bx, by};
;         }
;     }
; }
; __device__ __forceinline__ void mla_prologue(LAS unsigned char* lds, int tid, const bf16_t* QM, const bf16_t* KN, const bf16_t* KR, const bf16_t* VM, AU u, bf16x8 (&qr)[6]) {
;     asm volatile("" : "+v"(tid));
;     MLA_ADDR(u)
;     const bf16_t* Qw = QM + (rowb + q0 + wid * 32) * 768 + h * 96;
; #pragma unroll
;     for (int d0 = 0; d0 < 6; ++d0) qr[d0] = *(const GAS bf16x8*)(Qw + (size_t)r32 * 768 + d0 * 16 + hi * 8);
; #pragma unroll
;     for (int j = 0; j < 5; ++j) if (j < NT) mla_issue(lds, wid, ksrc, rsrc, vsrc, j);
; __device__ __forceinline__ void mla_unit(LAS unsigned char* lds, int tid, const bf16_t* QM, const bf16_t* KN, const bf16_t* KR, const bf16_t* VM, bf16_t* OA, float* OSS, AU u, bool has_next, AU nx, bf16x8 (&qr)[6]) {
;     ...
;     store_o(orow, o0, o1, hi2, 1.0f / lsum, oss);
;     asm volatile("s_waitcnt lgkmcnt(0)\n\ts_barrier" ::: "memory");
;     if (has_next) mla_prologue(lds, tid, QM, KN, KR, VM, nx, qr);
.LBB0_859:
	s_or_b64 exec, exec, s[8:9]
	v_readlane_b32 s8, v255, 36
	v_lshlrev_b64 v[4:5], 11, v[4:5]
	v_readlane_b32 s9, v255, 37
	s_lshl_b32 s88, s7, 1
	v_lshlrev_b32_e32 v0, 4, v209
	v_lshl_add_u64 v[4:5], s[8:9], 0, v[4:5]
	v_lshl_add_u64 v[4:5], v[4:5], 0, s[88:89]
	v_lshl_add_u64 v[8:9], v[4:5], 0, v[0:1]
	v_pk_mul_f32 v[4:5], v[48:49], v[2:3] op_sel_hi:[1,0]
	v_pk_mul_f32 v[6:7], v[50:51], v[2:3] op_sel_hi:[1,0]
	v_cvt_pk_bf16_f32 v4, v4, v5
	v_cvt_pk_bf16_f32 v5, v6, v7
	v_pk_mul_f32 v[6:7], v[52:53], v[2:3] op_sel_hi:[1,0]
	v_pk_mul_f32 v[10:11], v[54:55], v[2:3] op_sel_hi:[1,0]
	v_cvt_pk_bf16_f32 v6, v6, v7
	v_cvt_pk_bf16_f32 v7, v10, v11
	s_nop 0
	v_permlane32_swap_b32_e32 v4, v6
	v_permlane32_swap_b32_e32 v5, v7
	global_store_dwordx4 v[8:9], v[4:7], off offset:1024
	v_pk_mul_f32 v[10:11], v[62:63], v[2:3] op_sel_hi:[1,0]
	s_add_i32 s3, s37, 1
	v_pk_mul_f32 v[4:5], v[56:57], v[2:3] op_sel_hi:[1,0]
	v_pk_mul_f32 v[6:7], v[58:59], v[2:3] op_sel_hi:[1,0]
	v_cvt_pk_bf16_f32 v4, v4, v5
	v_cvt_pk_bf16_f32 v5, v6, v7
	v_pk_mul_f32 v[6:7], v[60:61], v[2:3] op_sel_hi:[1,0]
	s_cmp_lt_i32 s3, s2
	v_cvt_pk_bf16_f32 v6, v6, v7
	v_cvt_pk_bf16_f32 v7, v10, v11
	s_nop 0
	v_permlane32_swap_b32_e32 v4, v6
	v_permlane32_swap_b32_e32 v5, v7
	global_store_dwordx4 v[8:9], v[4:7], off offset:1056
	v_pk_mul_f32 v[10:11], v[22:23], v[2:3] op_sel_hi:[1,0]
	s_cselect_b64 s[8:9], -1, 0
	v_pk_mul_f32 v[4:5], v[16:17], v[2:3] op_sel_hi:[1,0]
	v_pk_mul_f32 v[6:7], v[18:19], v[2:3] op_sel_hi:[1,0]
	v_cvt_pk_bf16_f32 v4, v4, v5
	v_cvt_pk_bf16_f32 v5, v6, v7
	v_pk_mul_f32 v[6:7], v[20:21], v[2:3] op_sel_hi:[1,0]
	s_and_b64 vcc, exec, s[8:9]
	v_cvt_pk_bf16_f32 v6, v6, v7
	v_cvt_pk_bf16_f32 v7, v10, v11
	s_nop 0
	v_permlane32_swap_b32_e32 v4, v6
	v_permlane32_swap_b32_e32 v5, v7
	global_store_dwordx4 v[8:9], v[4:7], off offset:1088
	s_nop 1
	v_pk_mul_f32 v[4:5], v[24:25], v[2:3] op_sel_hi:[1,0]
	v_pk_mul_f32 v[6:7], v[26:27], v[2:3] op_sel_hi:[1,0]
	v_cvt_pk_bf16_f32 v4, v4, v5
	v_cvt_pk_bf16_f32 v5, v6, v7
	v_pk_mul_f32 v[6:7], v[28:29], v[2:3] op_sel_hi:[1,0]
	v_pk_mul_f32 v[2:3], v[30:31], v[2:3] op_sel_hi:[1,0]
	v_cvt_pk_bf16_f32 v6, v6, v7
	v_cvt_pk_bf16_f32 v7, v2, v3
	s_nop 0
	v_permlane32_swap_b32_e32 v4, v6
	v_permlane32_swap_b32_e32 v5, v7
	global_store_dwordx4 v[8:9], v[4:7], off offset:1120
	s_waitcnt lgkmcnt(0)
	s_barrier
	s_cbranch_vccz .LBB0_778
	s_cselect_b32 s6, s3, s37
	s_lshr_b32 s7, s6, 1
	s_mul_i32 s7, s7, s76
	s_add_i32 s7, s7, s79
	s_and_b32 s9, s7, 7
	s_ashr_i32 s8, s7, 6
	s_bfe_u32 s18, s7, 0x30003
	s_and_b32 s6, s6, 1
	s_xor_b32 s7, s9, 15
	s_cmp_eq_u32 s6, 0
	s_cselect_b32 s6, s7, s9
	v_readfirstlane_b32 s19, v189
	s_ashr_i32 s21, s19, 6
	s_ashr_i32 s9, s8, 31
	s_lshl_b64 s[8:9], s[8:9], 12
	s_lshl_b32 s7, s6, 8
	s_lshl_b32 s16, s21, 3
	s_lshl_b32 s22, s21, 5
	s_ashr_i32 s17, s16, 31
	s_and_b32 s20, s21, 3
	s_or_b32 s7, s8, s7
	s_ashr_i32 s23, s22, 31
	s_add_u32 s7, s7, s22
	s_addc_u32 s22, s9, s23
	s_mulk_i32 s22, 0x600
	s_mul_hi_u32 s23, s7, 0x600
	s_add_i32 s23, s23, s22
	s_mulk_i32 s7, 0x600
	s_add_u32 s7, s33, s7
	v_and_b32_e32 v0, 31, v189
	s_addc_u32 s23, s36, s23
	s_mul_i32 s22, s18, 0xc0
	s_add_u32 s22, s7, s22
	v_mul_u32_u24_e32 v0, 0x300, v0
	s_addc_u32 s23, s23, 0
	v_lshlrev_b32_e32 v0, 1, v0
	v_lshl_add_u64 v[2:3], s[22:23], 0, v[0:1]
	v_lshrrev_b32_e32 v0, 1, v189
	v_and_b32_e32 v0, 16, v0
	v_lshl_add_u64 v[2:3], v[2:3], 0, v[0:1]
	global_load_dwordx4 v[96:99], v[2:3], off nt
	global_load_dwordx4 v[100:103], v[2:3], off offset:32 nt
	global_load_dwordx4 v[104:107], v[2:3], off offset:64 nt
	global_load_dwordx4 v[108:111], v[2:3], off offset:96 nt
	global_load_dwordx4 v[112:115], v[2:3], off offset:128 nt
	global_load_dwordx4 v[116:119], v[2:3], off offset:160 nt
	v_and_b32_e32 v0, 63, v189
	v_or_b32_e32 v2, s8, v0
	v_mov_b32_e32 v3, s9
	v_lshlrev_b64 v[4:5], 10, v[2:3]
	v_lshl_add_u64 v[4:5], s[10:11], 0, v[4:5]
	s_lshl_b32 s88, s18, 7
	v_lshl_add_u64 v[4:5], v[4:5], 0, s[88:89]
	s_lshl_b32 s88, s20, 4
	s_lshl_b32 s7, s21, 10
	s_cmp_lt_i32 s21, 4
	v_lshl_add_u64 v[4:5], s[16:17], 1, v[4:5]
	s_cselect_b64 s[16:17], -1, 0
	s_add_i32 s7, s7, 0
	v_lshlrev_b64 v[2:3], 6, v[2:3]
	s_cmp_gt_i32 s21, 3
	s_mov_b32 s21, m0
	s_mov_b32 m0, s7
	s_nop 0
	global_load_lds_dwordx4 v[4:5], off
	s_mov_b32 m0, s21
	v_lshl_add_u64 v[2:3], s[12:13], 0, v[2:3]
	v_lshl_add_u64 v[2:3], v[2:3], 0, s[88:89]
	s_cbranch_scc1 .LBB0_862
	s_add_i32 s21, s7, 0x2000
	s_mov_b32 s22, m0
	s_mov_b32 m0, s21
	s_nop 0
	global_load_lds_dwordx4 v[2:3], off
	s_mov_b32 m0, s22

; #define GAS __attribute__((address_space(1)))
; #define LAS __attribute__((address_space(3)))
; #define GAS __attribute__((address_space(1)))
; #define SB_ISSUE(j) do { int kt_ = kt_hi - (j); kt_ = kt_ < 0 ? 0 : kt_; LAS unsigned char* sl_ = lds + ((j) % NS) * 16384 + wid * 1024; \
;         dma16(ksrc + (size_t)kt_ * 64 * 1536, sl_); dma16(vsrc + (size_t)kt_ * 64 * 1536, sl_ + 8192); } while (0)
; __device__ __forceinline__ void sb_unit(LAS unsigned char* lds, int tid, const bf16_t* QKV, bf16_t* OA, float* OSS, int b, int h, int qb) {
;     asm volatile("" : "+v"(tid));
;     const int lane = tid & 63, r32 = lane & 31, hi = lane >> 5, wid = __builtin_amdgcn_readfirstlane(tid >> 6);
;     const size_t rowb = (size_t)b * SEQ; const int q0 = qb * 256;
;     const bf16_t* Qw = QKV + (rowb + q0 + wid * 32) * 1536 + h * 64;
;     const bf16_t* Kh = QKV + rowb * 1536 + 512 + h * 64; const bf16_t* Vh = Kh + 512;
;     const int kt_hi = (q0 >> 6) + 3, NT = kt_hi + 1, jd = 3 - (wid >> 1);
;     const bf16_t* ksrc = Kh + (size_t)lane * 1536 + wid * 8;
;     const bf16_t* vsrc = Vh + (size_t)(16 * (wid & 3) + (lane >> 2)) * 1536 + (wid >> 2) * 32 + (lane & 3) * 8;
;     ...
;     bf16x8 qr[4];
; #pragma unroll
;     for (int d0 = 0; d0 < 4; ++d0) qr[d0] = *(const GAS bf16x8*)(Qw + (size_t)r32 * 1536 + d0 * 16 + hi * 8);
; #pragma unroll
;     for (int j = 0; j < PF; ++j) SB_ISSUE(j);
;     asm volatile("" : "+v"(qr[0]), "+v"(qr[1]), "+v"(qr[2]), "+v"(qr[3]));
;     f32x16 o0 = {}, o1 = {}; float carry = 1.f; bool mydone = false;
;     const int q = q0 + wid * 32 + r32;
;     volatile LAS unsigned* flags = (volatile LAS unsigned*)(lds + FLAG_OFF);
;     const int vpo = ((lane >> 4) & 1) * 32 + (lane & 3) * 8 + (4 * hi + ((lane & 15) >> 2)) * 64;
.LBB0_876:
	v_mov_b32_e32 v8, v188
	s_ashr_i32 s8, s79, 7
	s_and_b32 s2, s78, 15
	v_readfirstlane_b32 s13, v8
	s_and_b32 s12, s79, 15
	s_ashr_i32 s14, s13, 6
	s_ashr_i32 s9, s8, 31
	s_lshl_b32 s95, s2, 2
	s_lshl_b64 s[90:91], s[8:9], 12
	s_lshl_b32 s2, s12, 8
	s_lshl_b32 s3, s14, 5
	s_bfe_u32 s94, s79, 0x30004
	v_writelane_b32 v255, s2, 42
	s_or_b32 s2, s90, s2
	s_ashr_i32 s6, s3, 31
	s_add_u32 s2, s2, s3
	s_addc_u32 s6, s91, s6
	s_mulk_i32 s6, 0xc00
	s_mul_hi_u32 s7, s2, 0xc00
	s_add_i32 s7, s7, s6
	s_mulk_i32 s2, 0xc00
	v_readlane_b32 s10, v255, 40
	s_add_u32 s2, s10, s2
	v_readlane_b32 s11, v255, 41
	v_and_b32_e32 v115, 31, v8
	s_addc_u32 s7, s11, s7
	s_lshl_b32 s6, s94, 6
	s_lshl_b32 s9, s94, 7
	v_writelane_b32 v255, s6, 43
	s_add_u32 s6, s2, s9
	v_mul_u32_u24_e32 v0, 0x600, v115
	v_bfe_u32 v9, v8, 5, 1
	s_addc_u32 s7, s7, 0
	v_lshlrev_b32_e32 v0, 1, v0
	v_lshl_add_u64 v[2:3], s[6:7], 0, v[0:1]
	v_lshlrev_b32_e32 v0, 4, v9
	v_lshl_add_u64 v[2:3], v[2:3], 0, v[0:1]
	global_load_dwordx4 v[66:69], v[2:3], off offset:96 nt
	global_load_dwordx4 v[70:73], v[2:3], off offset:64 nt
	global_load_dwordx4 v[74:77], v[2:3], off offset:32 nt
	global_load_dwordx4 v[78:81], v[2:3], off nt
	s_mul_i32 s7, s8, 0xc00000
	s_mul_hi_i32 s6, s8, 0xc00000
	s_add_u32 s7, s10, s7
	s_addc_u32 s8, s11, s6
	s_add_u32 s6, s7, s9
	s_waitcnt lgkmcnt(8)
	v_and_b32_e32 v120, 63, v8
	s_addc_u32 s7, s8, 0
	s_lshl_b32 s10, s14, 4
	v_bfe_u32 v2, v8, 2, 4
	v_mul_u32_u24_e32 v0, 0x600, v120
	v_and_or_b32 v2, s10, 48, v2
	s_lshl_b32 s82, s12, 2
	s_lshl_b32 s8, s14, 3
	v_mul_u32_u24_e32 v4, 0x600, v2
	s_ashr_i32 s10, s13, 3
	v_lshlrev_b32_e32 v2, 3, v8
	v_lshlrev_b32_e32 v0, 1, v0
	s_ashr_i32 s9, s8, 31
	s_andn2_b32 s10, s10, 31
	v_and_b32_e32 v10, 24, v2
	s_or_b32 s15, s82, 3
	v_lshl_add_u64 v[2:3], s[6:7], 0, v[0:1]
	v_lshlrev_b32_e32 v0, 1, v4
	s_ashr_i32 s11, s10, 31
	v_lshl_add_u64 v[116:117], s[8:9], 1, v[2:3]
	v_lshl_add_u64 v[4:5], s[6:7], 0, v[0:1]
	s_mul_i32 s88, s15, 0x30000
	v_lshl_add_u64 v[4:5], s[10:11], 1, v[4:5]
	v_lshlrev_b32_e32 v0, 1, v10
	s_lshl_b32 s6, s14, 10
	v_lshl_add_u64 v[6:7], v[116:117], 0, s[88:89]
	v_lshl_add_u64 v[118:119], v[4:5], 0, v[0:1]
	s_add_i32 s33, s6, 0
	v_lshl_add_u64 v[6:7], v[6:7], 0, s[28:29]
	s_mov_b32 s6, m0
	s_mov_b32 m0, s33
	s_nop 0
	global_load_lds_dwordx4 v[6:7], off
	s_mov_b32 m0, s6
	v_lshl_add_u64 v[6:7], v[118:119], 0, s[88:89]
	s_add_i32 s6, s33, 0x2000
	v_lshl_add_u64 v[6:7], v[6:7], 0, s[30:31]
	s_mov_b32 s7, m0
	s_mov_b32 m0, s6
	s_nop 0
	global_load_lds_dwordx4 v[6:7], off
	s_mov_b32 m0, s7
	s_mul_i32 s6, s12, 0xc0000
	v_lshl_add_u64 v[2:3], v[116:117], 0, s[28:29]
	s_add_i32 s7, s33, 0x4000
	s_add_i32 s88, s6, 0x60000
	v_lshl_add_u64 v[4:5], v[118:119], 0, s[30:31]
	v_lshl_add_u64 v[6:7], v[2:3], 0, s[88:89]
	s_mov_b32 s8, m0
	s_mov_b32 m0, s7
	s_nop 0
	global_load_lds_dwordx4 v[6:7], off
	s_mov_b32 m0, s8
	s_add_i32 s7, s33, 0x6000
	v_lshl_add_u64 v[6:7], v[4:5], 0, s[88:89]
	s_mov_b32 s8, m0
	s_mov_b32 m0, s7
	s_nop 0
	global_load_lds_dwordx4 v[6:7], off
	s_mov_b32 m0, s8
	s_add_i32 s7, s33, 0x8000
	s_or_b32 s88, s6, 0x30000
	v_lshl_add_u64 v[2:3], v[2:3], 0, s[88:89]
	s_mov_b32 s8, m0
	s_mov_b32 m0, s7
	s_nop 0
	global_load_lds_dwordx4 v[2:3], off
	s_mov_b32 m0, s8
	s_add_i32 s7, s33, 0xa000
	v_lshl_add_u64 v[2:3], v[4:5], 0, s[88:89]
	s_mov_b32 s8, m0
	s_mov_b32 m0, s7
	s_nop 0
	global_load_lds_dwordx4 v[2:3], off
	s_mov_b32 m0, s8
	s_mov_b32 s7, s89
	v_lshl_add_u64 v[2:3], v[116:117], 0, s[6:7]
	v_lshl_add_u64 v[2:3], v[2:3], 0, s[28:29]
	s_add_i32 s8, s33, 0xc000
	s_mov_b32 s9, m0
	s_mov_b32 m0, s8
	s_nop 0
	global_load_lds_dwordx4 v[2:3], off
	s_mov_b32 m0, s9
	v_lshl_add_u64 v[2:3], v[118:119], 0, s[6:7]
	v_lshl_add_u64 v[2:3], v[2:3], 0, s[30:31]
	s_add_i32 s6, s33, 0xe000
	s_mov_b32 s7, m0
	s_mov_b32 m0, s6
	s_nop 0
	global_load_lds_dwordx4 v[2:3], off
	s_mov_b32 m0, s7
	v_sub_u32_e64 v0, s82, 1 clamp
	s_mov_b32 s7, 0x30000
	v_mul_lo_u32 v0, v0, s7
	v_lshl_add_u64 v[2:3], v[116:117], 0, v[0:1]
	v_lshl_add_u64 v[2:3], v[2:3], 0, s[28:29]
	s_add_i32 s6, s33, 0x10000
	s_mov_b32 s7, m0
	s_mov_b32 m0, s6
	s_nop 0
	global_load_lds_dwordx4 v[2:3], off
	s_mov_b32 m0, s7
	v_lshl_add_u64 v[2:3], v[118:119], 0, v[0:1]
	v_lshl_add_u64 v[2:3], v[2:3], 0, s[30:31]
	s_add_i32 s6, s33, 0x12000
	s_mov_b32 s7, m0
	s_mov_b32 m0, s6
	s_nop 0
	global_load_lds_dwordx4 v[2:3], off
	s_mov_b32 m0, s7
	v_lshlrev_b32_e32 v2, 4, v8
	v_lshlrev_b32_e32 v0, 1, v8
	v_and_b32_e32 v2, 0xc0, v2
	v_and_b32_e32 v0, 32, v0
	v_lshl_or_b32 v2, v9, 8, v2
	s_ashr_i32 s6, s13, 7
	v_or3_b32 v121, v2, v0, v10
	s_lshl_b32 s7, s14, 2
	v_lshlrev_b32_e32 v0, 2, v9
	v_or_b32_e32 v2, s3, v115
	s_add_i32 s88, s7, 0
	v_sub_u32_e32 v0, v2, v0
	s_lshl_b32 s7, s6, 6
	v_mov_b32_e32 v14, v1
	v_mov_b32_e32 v15, v1
	v_lshlrev_b32_e32 v114, 3, v9
	v_lshlrev_b32_e32 v123, 10, v9
	v_subrev_u32_e32 v124, s7, v0
	v_mov_b32_e32 v0, v1
	v_mov_b32_e32 v2, v1
	v_mov_b32_e32 v3, v1
	v_mov_b32_e32 v4, v1
	v_mov_b32_e32 v5, v1
	v_mov_b32_e32 v6, v1
	v_mov_b32_e32 v7, v1
	v_mov_b32_e32 v8, v1
	v_mov_b32_e32 v9, v1
	v_mov_b32_e32 v10, v1
	v_mov_b32_e32 v11, v1
	v_mov_b32_e32 v12, v1
	v_mov_b32_e32 v13, v1
	v_mov_b64_e32 v[32:33], v[14:15]
	v_mov_b64_e32 v[30:31], v[12:13]
	v_mov_b64_e32 v[28:29], v[10:11]
	v_mov_b64_e32 v[26:27], v[8:9]
	v_mov_b64_e32 v[24:25], v[6:7]
	v_mov_b64_e32 v[22:23], v[4:5]
	v_mov_b64_e32 v[20:21], v[2:3]
	v_mov_b64_e32 v[18:19], v[0:1]
	v_mov_b64_e32 v[16:17], v[14:15]
	s_mov_b32 s2, 5
	s_add_i32 s83, s82, 4
	s_add_i32 s88, s88, 0x20200
	v_lshlrev_b32_e32 v122, 4, v115
	s_mov_b32 s81, 0
	v_cmp_eq_u32_e64 s[8:9], 0, v120
	s_add_i32 s76, s95, 4
	s_sub_i32 s97, 0, s6
	v_mov_b32_e32 v125, 1.0
	s_mov_b64 s[10:11], 0
	s_mov_b32 s80, -2
	s_mov_b32 s77, 0
	s_mov_b32 s6, 0
	v_mov_b64_e32 v[14:15], v[12:13]
	v_mov_b64_e32 v[12:13], v[10:11]
	v_mov_b64_e32 v[10:11], v[8:9]
	v_mov_b64_e32 v[8:9], v[6:7]
	v_mov_b64_e32 v[6:7], v[4:5]
	v_mov_b64_e32 v[4:5], v[2:3]
	v_mov_b64_e32 v[2:3], v[0:1]
	s_waitcnt vmcnt(2)
	s_branch .LBB0_878

; #define LAS __attribute__((address_space(3)))
; __device__ __forceinline__ u32x4 pack8(f32x4 a, f32x4 b) { u32x4 w; w.x = pk2(a[0], a[1]); w.y = pk2(a[2], a[3]); w.z = pk2(b[0], b[1]); w.w = pk2(b[2], b[3]); return w; }
;     __device__ __forceinline__ void operator()(const f32x4 (&acc)[2][2][4][2], const Unit& u, int ui, int wr, int wc, int fr, int fq, LAS unsigned char* lds) const {
; #pragma unroll
;         for (int ai = 0; ai < 2; ++ai)
; #pragma unroll
;             for (int m = 0; m < 4; ++m) {
;                 const int row = u.pm * 256 + ai * 128 + wr * 64 + m * 16 + fr;
; #pragma unroll
;                 for (int bj = 0; bj < 2; ++bj) { const int c = u.pn * 256 + bj * 128 + wc * 32 + fq * 8;
;                     *(u32x4*)(O + (size_t)row * ldc + c) = pack8(acc[ai][bj][m][0], acc[ai][bj][m][1]); }
;             }
;     }
.LBB0_1253:
	v_mov_b32_e32 v135, v188
	s_lshl_b32 s35, s45, 8
	s_add_i32 s35, s35, s40
	v_and_or_b32 v136, v135, 15, s35
	s_lshl_b32 s35, s46, 8
	v_lshrrev_b32_e32 v135, 1, v135
	v_and_or_b32 v135, v135, 24, s35
	v_or_b32_e32 v138, s41, v135
	v_ashrrev_i32_e32 v137, 31, v136
	v_cvt_pk_bf16_f32 v114, v114, v115
	v_cvt_pk_bf16_f32 v115, v116, v117
	v_cvt_pk_bf16_f32 v116, v118, v119
	v_lshlrev_b64 v[118:119], 11, v[136:137]
	v_ashrrev_i32_e32 v139, 31, v138
	v_cvt_pk_bf16_f32 v117, v120, v121
	v_lshl_add_u64 v[118:119], s[18:19], 0, v[118:119]
	v_lshlrev_b64 v[120:121], 1, v[138:139]
	v_lshl_add_u64 v[118:119], v[118:119], 0, v[120:121]
	flat_store_dwordx4 v[118:119], v[114:117] nt
	v_cvt_pk_bf16_f32 v98, v98, v99
	v_cvt_pk_bf16_f32 v99, v100, v101
	v_cvt_pk_bf16_f32 v114, v122, v123
	v_cvt_pk_bf16_f32 v115, v124, v125
	v_cvt_pk_bf16_f32 v116, v126, v127
	v_cvt_pk_bf16_f32 v117, v128, v129
	flat_store_dwordx4 v[118:119], v[114:117] offset:256 nt
	v_cvt_pk_bf16_f32 v100, v102, v103
	v_cvt_pk_bf16_f32 v101, v104, v105
	v_or_b32_e32 v114, 16, v136
	v_ashrrev_i32_e32 v115, 31, v114
	v_lshlrev_b64 v[102:103], 11, v[114:115]
	v_lshl_add_u64 v[102:103], s[18:19], 0, v[102:103]
	v_lshl_add_u64 v[102:103], v[102:103], 0, v[120:121]
	flat_store_dwordx4 v[102:103], v[98:101] nt
	v_cvt_pk_bf16_f32 v66, v66, v67
	v_cvt_pk_bf16_f32 v67, v68, v69
	v_cvt_pk_bf16_f32 v98, v106, v107
	v_cvt_pk_bf16_f32 v99, v108, v109
	v_cvt_pk_bf16_f32 v100, v110, v111
	v_cvt_pk_bf16_f32 v101, v112, v113
	flat_store_dwordx4 v[102:103], v[98:101] offset:256 nt
	v_cvt_pk_bf16_f32 v68, v70, v71
	v_cvt_pk_bf16_f32 v69, v72, v73
	v_or_b32_e32 v98, 32, v136
	v_ashrrev_i32_e32 v99, 31, v98
	v_lshlrev_b64 v[70:71], 11, v[98:99]
	v_lshl_add_u64 v[70:71], s[18:19], 0, v[70:71]
	v_lshl_add_u64 v[70:71], v[70:71], 0, v[120:121]
	flat_store_dwordx4 v[70:71], v[66:69] nt
	v_cvt_pk_bf16_f32 v34, v34, v35
	v_cvt_pk_bf16_f32 v35, v36, v37
	v_cvt_pk_bf16_f32 v66, v74, v75
	v_cvt_pk_bf16_f32 v67, v76, v77
	v_cvt_pk_bf16_f32 v68, v78, v79
	v_cvt_pk_bf16_f32 v69, v80, v81
	flat_store_dwordx4 v[70:71], v[66:69] offset:256 nt
	v_cvt_pk_bf16_f32 v36, v38, v39
	v_cvt_pk_bf16_f32 v37, v40, v41
	v_or_b32_e32 v66, 48, v136
	v_ashrrev_i32_e32 v67, 31, v66
	v_lshlrev_b64 v[38:39], 11, v[66:67]
	v_lshl_add_u64 v[38:39], s[18:19], 0, v[38:39]
	v_lshl_add_u64 v[38:39], v[38:39], 0, v[120:121]
	flat_store_dwordx4 v[38:39], v[34:37] nt
	v_cvt_pk_bf16_f32 v18, v18, v19
	v_cvt_pk_bf16_f32 v19, v20, v21
	v_cvt_pk_bf16_f32 v34, v42, v43
	v_cvt_pk_bf16_f32 v35, v44, v45
	v_cvt_pk_bf16_f32 v36, v46, v47
	v_cvt_pk_bf16_f32 v37, v48, v49
	flat_store_dwordx4 v[38:39], v[34:37] offset:256 nt
	v_add_u32_e32 v38, 0x80, v136
	v_ashrrev_i32_e32 v39, 31, v38
	v_lshlrev_b64 v[38:39], 11, v[38:39]
	v_lshl_add_u64 v[38:39], s[18:19], 0, v[38:39]
	v_cvt_pk_bf16_f32 v34, v82, v83
	v_cvt_pk_bf16_f32 v35, v84, v85
	v_cvt_pk_bf16_f32 v36, v86, v87
	v_cvt_pk_bf16_f32 v37, v88, v89
	v_lshl_add_u64 v[38:39], v[38:39], 0, v[120:121]
	flat_store_dwordx4 v[38:39], v[34:37] nt
	v_cvt_pk_bf16_f32 v20, v22, v23
	v_cvt_pk_bf16_f32 v21, v24, v25
	v_cvt_pk_bf16_f32 v34, v90, v91
	v_cvt_pk_bf16_f32 v35, v92, v93
	v_cvt_pk_bf16_f32 v36, v94, v95
	v_cvt_pk_bf16_f32 v37, v96, v97
	flat_store_dwordx4 v[38:39], v[34:37] offset:256 nt
	v_add_u32_e32 v38, 0x90, v136
	v_ashrrev_i32_e32 v39, 31, v38
	v_lshlrev_b64 v[38:39], 11, v[38:39]
	v_lshl_add_u64 v[38:39], s[18:19], 0, v[38:39]
	v_cvt_pk_bf16_f32 v34, v50, v51
	v_cvt_pk_bf16_f32 v35, v52, v53
	v_cvt_pk_bf16_f32 v36, v54, v55
	v_cvt_pk_bf16_f32 v37, v56, v57
	v_lshl_add_u64 v[38:39], v[38:39], 0, v[120:121]
	flat_store_dwordx4 v[38:39], v[34:37] nt
	v_cvt_pk_bf16_f32 v2, v2, v3
	v_cvt_pk_bf16_f32 v3, v4, v5
	v_cvt_pk_bf16_f32 v34, v58, v59
	v_cvt_pk_bf16_f32 v35, v60, v61
	v_cvt_pk_bf16_f32 v36, v62, v63
	v_cvt_pk_bf16_f32 v37, v64, v65
	flat_store_dwordx4 v[38:39], v[34:37] offset:256 nt
	v_cvt_pk_bf16_f32 v4, v6, v7
	v_cvt_pk_bf16_f32 v5, v8, v9
	v_add_u32_e32 v34, 0xa0, v136
	v_ashrrev_i32_e32 v35, 31, v34
	v_lshlrev_b64 v[22:23], 11, v[34:35]
	v_lshl_add_u64 v[22:23], s[18:19], 0, v[22:23]
	v_lshl_add_u64 v[22:23], v[22:23], 0, v[120:121]
	flat_store_dwordx4 v[22:23], v[18:21] nt
	s_and_b64 vcc, exec, s[10:11]
	s_mov_b64 s[10:11], -1
	v_cvt_pk_bf16_f32 v18, v26, v27
	v_cvt_pk_bf16_f32 v19, v28, v29
	v_cvt_pk_bf16_f32 v20, v30, v31
	v_cvt_pk_bf16_f32 v21, v32, v33
	flat_store_dwordx4 v[22:23], v[18:21] offset:256 nt
	v_readlane_b32 s55, v255, 18
	v_mov_b64_e32 v[248:249], v[250:251]
	v_add_u32_e32 v18, 0xb0, v136
	v_ashrrev_i32_e32 v19, 31, v18
	v_lshlrev_b64 v[6:7], 11, v[18:19]
	v_lshl_add_u64 v[6:7], s[18:19], 0, v[6:7]
	v_lshl_add_u64 v[6:7], v[6:7], 0, v[120:121]
	flat_store_dwordx4 v[6:7], v[2:5] nt
	v_mov_b64_e32 v[238:239], 0x47f
	v_mov_b32_e32 v234, 0x30000
	v_cvt_pk_bf16_f32 v2, v10, v11
	v_cvt_pk_bf16_f32 v3, v12, v13
	v_cvt_pk_bf16_f32 v4, v14, v15
	v_cvt_pk_bf16_f32 v5, v16, v17
	v_mov_b32_e32 v235, v252
	v_mov_b32_e32 v251, 0x260
	v_mov_b32_e32 v236, 0x358637bd
	flat_store_dwordx4 v[6:7], v[2:5] offset:256 nt
	s_cbranch_vccnz .LBB0_1242
	ds_read_b128 v[2:5], v132
	s_andn2_b64 vcc, exec, s[16:17]
	s_cbranch_vccnz .LBB0_1241
	s_barrier
	s_branch .LBB0_1241
